# W1 conversion hosted in the G1 phase instead of the tail phase: odd-XCD workgroups convert before their G1 units, even-XCD ones after
# baseline (speedup 1.0000x reference)
; #define LAS __attribute__((address_space(3)))
; #define REP(n) for (int rep_ = 0; rep_ < 1 + ((REPMASK >> (n)) & 1); ++rep_)
; #define IN(k) (lo <= (k) && (k) < hi && ((F = make_frame((LAS unsigned char*)lds_raw, wv)), true))
; DI void phase_expert_weights(const Frame& F, int l, int which) {
;     LAS float* scr = (LAS float*)(F.lds + F.wave * 16384);
;     unsigned char* ws = F.ws;
;     if (which == 0) {
;         constexpr int IPM = (D / 64) * (2048 / 32);
;         for (int it = F.gw; it < NE * IPM; it += F.NGW) { const int mtx = l * NE + it / IPM, r = it % IPM;
;             transpose_item(F.ap->in[32] + (size_t)mtx * D * 2048, D, 2048, (bf16_t*)(ws + WS_W1 + (size_t)mtx * 2048 * D), 3, scr, r, F.lane); }
; __global__ void __launch_bounds__(NTHR, 2) fwd_kernel(Args args) {
;     ...
;         const int pb = PH_BASE + l * PH_PER_LAYER, j = l >> 1; const bool even = (l & 1) == 0;
;         REP(2) if (PM(2)) if (IN(pb + 0)) {
.LBB0_166:
	s_lshr_b32 s4, s28, 1
	v_writelane_b32 v253, s4, 54
	s_lshl_b32 s8, s28, 4
	s_or_b32 s2, s8, 2
	v_writelane_b32 v253, s5, 55
	s_mov_b32 s4, s28
	v_writelane_b32 v253, s4, 56
	s_nop 1
	v_writelane_b32 v253, s5, 57
	s_and_b32 s4, s28, 1
	s_cmp_eq_u32 s4, 0
	s_cselect_b64 s[56:57], -1, 0
	s_cmp_eq_u32 s4, 1
	s_cselect_b64 s[38:39], -1, 0
	s_cmp_le_i32 s96, s2
	s_cselect_b64 s[4:5], -1, 0
	s_cmp_lt_i32 s2, s97
	s_cselect_b64 s[6:7], -1, 0
	s_and_b64 s[4:5], s[4:5], s[6:7]
	s_or_b32 s17, s8, 3
	s_cmp_lt_i32 s17, s97
	v_writelane_b32 v253, s8, 58
	s_cselect_b64 s[40:41], -1, 0
	s_and_b64 vcc, exec, s[4:5]
	s_cbranch_vccz .LBB0_236
	s_bitcmp0_b32 s94, 0
	s_cbranch_scc1 .Lg1p_skip
	s_mov_b32 s22, s10
	s_mov_b32 s23, s17
	s_mov_b64 s[24:25], s[38:39]
	v_readlane_b32 s30, v253, 58
	s_nop 0
	s_lshl_b32 s30, s30, 1
	v_mov_b32_e32 v150, v0
	v_mov_b32_e32 v151, v1
	v_mov_b32_e32 v152, v2
	v_mov_b32_e32 v153, v3
	v_mov_b32_e32 v154, v4
	v_mov_b32_e32 v155, v5
	v_mov_b32_e32 v156, v6
	v_mov_b32_e32 v157, v7
	v_mov_b32_e32 v158, v8
	v_mov_b32_e32 v159, v9
	v_mov_b32_e32 v160, v10
	v_mov_b32_e32 v161, v11
	v_mov_b32_e32 v162, v12
	v_mov_b32_e32 v163, v13
	v_mov_b32_e32 v164, v14
	v_mov_b32_e32 v165, v15
	v_mov_b32_e32 v166, v16
	v_mov_b32_e32 v167, v17
	v_mov_b32_e32 v168, v18
	v_mov_b32_e32 v169, v19
	v_mov_b32_e32 v170, v20
	v_mov_b32_e32 v171, v21
	v_mov_b32_e32 v172, v22
	v_mov_b32_e32 v173, v23
	v_mov_b32_e32 v174, v24
	v_mov_b32_e32 v175, v25
	v_mov_b32_e32 v176, v26
	v_mov_b32_e32 v177, v27
	v_mov_b32_e32 v178, v28
	v_mov_b32_e32 v179, v29
	v_mov_b32_e32 v180, v30
	v_mov_b32_e32 v181, v31
	v_mov_b32_e32 v182, v32
	v_mov_b32_e32 v183, v33
	v_mov_b32_e32 v184, v34
	v_mov_b32_e32 v185, v35
	v_mov_b32_e32 v186, v36
	v_mov_b32_e32 v187, v37
	v_mov_b32_e32 v188, v38
	v_mov_b32_e32 v189, v39
	v_mov_b32_e32 v190, v40
	v_mov_b32_e32 v191, v41
	v_mov_b32_e32 v194, v192
	s_mov_b64 s[4:5], s[58:59]
	v_readlane_b32 s2, v252, 0
	s_waitcnt lgkmcnt(0)
	v_mbcnt_lo_u32_b32 v0, -1, 0
	v_mbcnt_hi_u32_b32 v0, -1, v0
	s_mov_b32 s6, s94
	v_add_u32_e32 v1, s2, v0
	s_mov_b32 s2, s60
	s_and_b32 s7, s2, 7
	s_cmp_lg_u32 s7, 0
	v_readfirstlane_b32 s7, v1
	s_cbranch_scc1 .Lg1p_1107
	s_ashr_i32 s9, s6, 31
	s_lshr_b32 s9, s9, 29
	s_add_i32 s9, s6, s9
	s_ashr_i32 s10, s9, 3
	s_and_b32 s9, s9, -8
	s_ashr_i32 s8, s2, 3
	s_sub_i32 s6, s6, s9
	s_mul_i32 s6, s8, s6
	s_add_i32 s6, s6, s10

; #define LAS __attribute__((address_space(3)))
; DI unsigned pk2(float lo, float hi) { return f2bf(lo) | (f2bf(hi) << 16); }
; DI unsigned pk_fp8x4(float a, float b, float c, float d) { int p = 0; p = __builtin_amdgcn_cvt_pk_fp8_f32(a, b, p, false); p = __builtin_amdgcn_cvt_pk_fp8_f32(c, d, p, true); return (unsigned)p; }
; #define LDS_WAIT() asm volatile("s_waitcnt lgkmcnt(0)" ::: "memory")
; DI void transpose_item(const float* W, int K, int N, bf16_t* WT, int mode, LAS float* scr, int item, int lane) {
;     const int nblk = N / 32, kb = item / nblk, nb = item % nblk, k0 = 64 * kb, n0 = 32 * nb;
;     { const int rr = lane >> 3, c4 = lane & 7; f32x4 v[8];
; #pragma unroll
;       for (int i = 0; i < 8; ++i) v[i] = *(const f32x4*)(W + (size_t)(k0 + 8 * i + rr) * N + n0 + 4 * c4);
; #pragma unroll
;       for (int i = 0; i < 8; ++i) { LAS float* d = scr + (8 * i + rr) * 33 + 4 * c4; d[0] = v[i].x; d[1] = v[i].y; d[2] = v[i].z; d[3] = v[i].w; } }
;     LDS_WAIT(); asm volatile("" ::: "memory");
;     const int c = lane & 7;
; #pragma unroll
;     for (int j = 0; j < 4; ++j) { const int n = (lane >> 3) + 8 * j; const LAS float* s = scr + (8 * c) * 33 + n;
;         const int row = (mode & 1) ? w1_row(n0 + n) : (n0 + n);
;         if (mode & 2) { u32x2 o; o.x = pk_fp8x4(s[0 * 33] * W8_SCALE, s[1 * 33] * W8_SCALE, s[2 * 33] * W8_SCALE, s[3 * 33] * W8_SCALE); o.y = pk_fp8x4(s[4 * 33] * W8_SCALE, s[5 * 33] * W8_SCALE, s[6 * 33] * W8_SCALE, s[7 * 33] * W8_SCALE);
;             *(u32x2*)((unsigned char*)WT + (size_t)row * K + k0 + 8 * c) = o; }
;         else { u32x4 o; o.x = pk2(s[0 * 33], s[1 * 33]); o.y = pk2(s[2 * 33], s[3 * 33]); o.z = pk2(s[4 * 33], s[5 * 33]); o.w = pk2(s[6 * 33], s[7 * 33]);
;             *(u32x4*)(WT + (size_t)row * K + k0 + 8 * c) = o; } }
;     LDS_WAIT(); asm volatile("" ::: "memory");
; }
.Lg1p_1109:
	s_ashr_i32 s2, s6, 31
	s_lshr_b32 s2, s2, 22
	s_add_i32 s2, s6, s2
	s_ashr_i32 s8, s2, 10
	s_add_i32 s8, s8, s30
	s_and_b32 s2, s2, 0xfc00
	s_ashr_i32 s9, s8, 31
	s_sub_i32 s2, s6, s2
	s_lshl_b64 s[12:13], s[8:9], 23
	s_add_u32 s17, s36, s12
	s_addc_u32 s19, s37, s13
	s_lshl_b64 s[8:9], s[8:9], 21
	s_add_u32 s8, s5, s8
	s_sext_i32_i16 s10, s2
	s_addc_u32 s9, s7, s9
	s_bfe_u32 s10, s10, 0x60019
	s_add_i32 s10, s2, s10
	s_sext_i32_i16 s12, s10
	s_and_b32 s10, s10, 0xffc0
	s_sub_i32 s2, s2, s10
	s_sext_i32_i16 s2, s2
	s_lshl_b32 s38, s2, 5
	s_ashr_i32 s39, s38, 31
	s_and_b32 s10, s12, 0xffffffc0
	s_lshl_b64 s[12:13], s[38:39], 2
	v_or_b32_e32 v0, s10, v30
	s_add_u32 s12, s17, s12
	s_addc_u32 s13, s19, s13
	v_ashrrev_i32_e32 v1, 31, v0
	v_lshl_add_u64 v[2:3], s[12:13], 0, v[192:193]
	v_lshlrev_b64 v[4:5], 13, v[0:1]
	v_lshl_add_u64 v[4:5], v[2:3], 0, v[4:5]
	global_load_dwordx4 v[38:41], v[4:5], off
	v_or_b32_e32 v4, 8, v0
	v_ashrrev_i32_e32 v5, 31, v4
	v_lshlrev_b64 v[4:5], 13, v[4:5]
	v_lshl_add_u64 v[4:5], v[2:3], 0, v[4:5]
	global_load_dwordx4 v[24:27], v[4:5], off
	v_or_b32_e32 v4, 16, v0
	v_ashrrev_i32_e32 v5, 31, v4
	v_lshlrev_b64 v[4:5], 13, v[4:5]
	v_lshl_add_u64 v[4:5], v[2:3], 0, v[4:5]
	global_load_dwordx4 v[20:23], v[4:5], off
	v_or_b32_e32 v4, 24, v0
	v_ashrrev_i32_e32 v5, 31, v4
	v_lshlrev_b64 v[4:5], 13, v[4:5]
	v_lshl_add_u64 v[4:5], v[2:3], 0, v[4:5]
	global_load_dwordx4 v[16:19], v[4:5], off
	v_or_b32_e32 v4, 32, v0
	v_ashrrev_i32_e32 v5, 31, v4
	v_lshlrev_b64 v[4:5], 13, v[4:5]
	v_lshl_add_u64 v[4:5], v[2:3], 0, v[4:5]
	global_load_dwordx4 v[12:15], v[4:5], off
	v_or_b32_e32 v4, 40, v0
	v_ashrrev_i32_e32 v5, 31, v4
	v_lshlrev_b64 v[4:5], 13, v[4:5]
	v_lshl_add_u64 v[4:5], v[2:3], 0, v[4:5]
	global_load_dwordx4 v[8:11], v[4:5], off
	v_or_b32_e32 v4, 48, v0
	v_ashrrev_i32_e32 v5, 31, v4
	v_lshlrev_b64 v[4:5], 13, v[4:5]
	v_or_b32_e32 v0, 56, v0
	v_lshl_add_u64 v[4:5], v[2:3], 0, v[4:5]
	v_ashrrev_i32_e32 v1, 31, v0
	global_load_dwordx4 v[4:7], v[4:5], off
	v_lshlrev_b64 v[0:1], 13, v[0:1]
	v_lshl_add_u64 v[0:1], v[2:3], 0, v[0:1]
	global_load_dwordx4 v[0:3], v[0:1], off
	v_add_u32_e32 v37, 0x420, v36
	s_ashr_i32 s2, s10, 31
	s_add_u32 s8, s8, s10
	s_addc_u32 s9, s9, s2
	s_and_b32 s2, s38, 0xffffff00
	s_add_i32 s6, s6, s4
	s_cmp_lt_i32 s6, 0x8000
	s_waitcnt vmcnt(0)
	ds_write2_b32 v36, v38, v39 offset1:1
	ds_write2_b32 v36, v40, v41 offset0:2 offset1:3
	ds_write2_b32 v37, v24, v25 offset1:1
	v_add_u32_e32 v24, 0x428, v36
	ds_write2_b32 v24, v26, v27 offset1:1
	v_add_u32_e32 v24, 0x840, v36
	ds_write2_b32 v24, v20, v21 offset1:1
	v_add_u32_e32 v20, 0x848, v36
	ds_write2_b32 v20, v22, v23 offset1:1
	v_add_u32_e32 v20, 0xc60, v36
	ds_write2_b32 v20, v16, v17 offset1:1
	v_add_u32_e32 v16, 0xc68, v36
	ds_write2_b32 v16, v18, v19 offset1:1
	v_add_u32_e32 v16, 0x1080, v36
	ds_write2_b32 v16, v12, v13 offset1:1
	v_add_u32_e32 v12, 0x1088, v36
	ds_write2_b32 v12, v14, v15 offset1:1
	v_add_u32_e32 v12, 0x14a0, v36
	v_mov_b32_e32 v13, v193
	ds_write2_b32 v12, v8, v9 offset1:1
	v_add_u32_e32 v8, 0x14a8, v36
	ds_write2_b32 v8, v10, v11 offset1:1
	v_add_u32_e32 v8, 0x18c0, v36
	v_mov_b32_e32 v12, v193
	ds_write2_b32 v8, v4, v5 offset1:1
	v_add_u32_e32 v4, 0x18c8, v36
	ds_write2_b32 v4, v6, v7 offset1:1
	v_add_u32_e32 v4, 0x1ce0, v36
	ds_write2_b32 v4, v0, v1 offset1:1
	v_add_u32_e32 v0, 0x1ce8, v36
	ds_write2_b32 v0, v2, v3 offset1:1
	s_waitcnt lgkmcnt(0)
	ds_read2_b32 v[4:5], v35 offset1:8
	ds_read2_b32 v[6:7], v35 offset0:33 offset1:41
	ds_read2_b32 v[14:15], v35 offset0:132 offset1:140
	ds_read2_b32 v[16:17], v35 offset0:165 offset1:173
	ds_read2_b32 v[8:9], v35 offset0:66 offset1:74
	ds_read2_b32 v[10:11], v35 offset0:99 offset1:107
	s_waitcnt lgkmcnt(5)
	v_mul_f32_e32 v3, 0x42800000, v4
	s_waitcnt lgkmcnt(4)
	v_mul_f32_e32 v4, 0x42800000, v6
	ds_read2_b32 v[18:19], v35 offset0:198 offset1:206
	ds_read2_b32 v[20:21], v35 offset0:231 offset1:239
	v_cvt_pk_fp8_f32 v12, v3, v4
	s_waitcnt lgkmcnt(5)
	v_mul_f32_e32 v3, 0x42800000, v14
	s_waitcnt lgkmcnt(4)
	v_mul_f32_e32 v4, 0x42800000, v16
	v_cvt_pk_fp8_f32 v13, v3, v4
	v_or_b32_e32 v2, s38, v30
	v_lshrrev_b32_e32 v2, 1, v2
	s_waitcnt lgkmcnt(3)
	v_mul_f32_e32 v6, 0x42800000, v8
	s_waitcnt lgkmcnt(2)
	v_mul_f32_e32 v8, 0x42800000, v10
	v_and_b32_e32 v2, 0x73, v2
	v_cvt_pk_fp8_f32 v12, v6, v8 op_sel:[0,0,1]
	s_waitcnt lgkmcnt(1)
	v_mul_f32_e32 v6, 0x42800000, v18
	s_waitcnt lgkmcnt(0)
	v_mul_f32_e32 v8, 0x42800000, v20
	v_or3_b32 v2, s2, v2, v34
	v_cvt_pk_fp8_f32 v13, v6, v8 op_sel:[0,0,1]
	v_ashrrev_i32_e32 v3, 31, v2
	v_lshl_add_u64 v[0:1], s[8:9], 0, v[28:29]
	v_lshlrev_b64 v[2:3], 10, v[2:3]
	v_lshl_add_u64 v[2:3], v[0:1], 0, v[2:3]
	global_store_dwordx2 v[2:3], v[12:13], off
	v_mul_f32_e32 v3, 0x42800000, v5
	v_mul_f32_e32 v5, 0x42800000, v7
	v_mov_b32_e32 v4, v193
	v_cvt_pk_fp8_f32 v4, v3, v5
	v_mul_f32_e32 v6, 0x42800000, v9
	v_mul_f32_e32 v7, 0x42800000, v11
	v_mul_f32_e32 v3, 0x42800000, v15
	v_cvt_pk_fp8_f32 v4, v6, v7 op_sel:[0,0,1]
	v_mul_f32_e32 v6, 0x42800000, v17
	v_mov_b32_e32 v5, v193
	v_cvt_pk_fp8_f32 v5, v3, v6
	v_or_b32_e32 v2, s38, v31
	v_lshrrev_b32_e32 v2, 1, v2
	v_and_b32_e32 v2, 0x77, v2
	v_mul_f32_e32 v7, 0x42800000, v19
	v_mul_f32_e32 v8, 0x42800000, v21
	v_or3_b32 v2, s2, v2, v34
	v_cvt_pk_fp8_f32 v5, v7, v8 op_sel:[0,0,1]
	v_ashrrev_i32_e32 v3, 31, v2
	v_lshlrev_b64 v[2:3], 10, v[2:3]
	v_lshl_add_u64 v[2:3], v[0:1], 0, v[2:3]
	global_store_dwordx2 v[2:3], v[4:5], off
	ds_read2_b32 v[4:5], v35 offset0:16 offset1:24
	ds_read2_b32 v[6:7], v35 offset0:49 offset1:57
	ds_read2_b32 v[14:15], v35 offset0:148 offset1:156
	ds_read2_b32 v[16:17], v35 offset0:181 offset1:189
	ds_read2_b32 v[8:9], v35 offset0:82 offset1:90
	ds_read2_b32 v[10:11], v35 offset0:115 offset1:123
	s_waitcnt lgkmcnt(5)
; #define LAS __attribute__((address_space(3)))
; DI unsigned pk2(float lo, float hi) { return f2bf(lo) | (f2bf(hi) << 16); }
; DI unsigned pk_fp8x4(float a, float b, float c, float d) { int p = 0; p = __builtin_amdgcn_cvt_pk_fp8_f32(a, b, p, false); p = __builtin_amdgcn_cvt_pk_fp8_f32(c, d, p, true); return (unsigned)p; }
; #define LDS_WAIT() asm volatile("s_waitcnt lgkmcnt(0)" ::: "memory")
; DI void transpose_item(const float* W, int K, int N, bf16_t* WT, int mode, LAS float* scr, int item, int lane) {
;     ...
;     for (int j = 0; j < 4; ++j) { const int n = (lane >> 3) + 8 * j; const LAS float* s = scr + (8 * c) * 33 + n;
;         const int row = (mode & 1) ? w1_row(n0 + n) : (n0 + n);
;         if (mode & 2) { u32x2 o; o.x = pk_fp8x4(s[0 * 33] * W8_SCALE, s[1 * 33] * W8_SCALE, s[2 * 33] * W8_SCALE, s[3 * 33] * W8_SCALE); o.y = pk_fp8x4(s[4 * 33] * W8_SCALE, s[5 * 33] * W8_SCALE, s[6 * 33] * W8_SCALE, s[7 * 33] * W8_SCALE);
;             *(u32x2*)((unsigned char*)WT + (size_t)row * K + k0 + 8 * c) = o; }
;         else { u32x4 o; o.x = pk2(s[0 * 33], s[1 * 33]); o.y = pk2(s[2 * 33], s[3 * 33]); o.z = pk2(s[4 * 33], s[5 * 33]); o.w = pk2(s[6 * 33], s[7 * 33]);
;             *(u32x4*)(WT + (size_t)row * K + k0 + 8 * c) = o; } }
;     LDS_WAIT(); asm volatile("" ::: "memory");
; }
	v_mul_f32_e32 v3, 0x42800000, v4
	s_waitcnt lgkmcnt(4)
	v_mul_f32_e32 v4, 0x42800000, v6
	v_mov_b32_e32 v12, v193
	ds_read2_b32 v[18:19], v35 offset0:214 offset1:222
	ds_read2_b32 v[20:21], v35 offset0:247 offset1:255
	v_cvt_pk_fp8_f32 v12, v3, v4
	s_waitcnt lgkmcnt(5)
	v_mul_f32_e32 v3, 0x42800000, v14
	s_waitcnt lgkmcnt(4)
	v_mul_f32_e32 v4, 0x42800000, v16
	v_mov_b32_e32 v13, v193
	v_cvt_pk_fp8_f32 v13, v3, v4
	v_or_b32_e32 v2, s38, v32
	v_lshrrev_b32_e32 v2, 1, v2
	s_waitcnt lgkmcnt(3)
	v_mul_f32_e32 v6, 0x42800000, v8
	s_waitcnt lgkmcnt(2)
	v_mul_f32_e32 v8, 0x42800000, v10
	v_and_b32_e32 v2, 0x7b, v2
	v_cvt_pk_fp8_f32 v12, v6, v8 op_sel:[0,0,1]
	s_waitcnt lgkmcnt(1)
	v_mul_f32_e32 v6, 0x42800000, v18
	s_waitcnt lgkmcnt(0)
	v_mul_f32_e32 v8, 0x42800000, v20
	v_or3_b32 v2, s2, v2, v34
	v_cvt_pk_fp8_f32 v13, v6, v8 op_sel:[0,0,1]
	v_ashrrev_i32_e32 v3, 31, v2
	v_lshlrev_b64 v[2:3], 10, v[2:3]
	v_lshl_add_u64 v[2:3], v[0:1], 0, v[2:3]
	global_store_dwordx2 v[2:3], v[12:13], off
	v_or_b32_e32 v2, s38, v33
	v_bfe_u32 v2, v2, 1, 7
	v_or3_b32 v4, s2, v2, v34
	v_mul_f32_e32 v3, 0x42800000, v5
	v_mul_f32_e32 v5, 0x42800000, v7
	v_mov_b32_e32 v2, v193
	v_cvt_pk_fp8_f32 v2, v3, v5
	v_mul_f32_e32 v6, 0x42800000, v9
	v_mul_f32_e32 v7, 0x42800000, v11
	v_mul_f32_e32 v5, 0x42800000, v15
	v_cvt_pk_fp8_f32 v2, v6, v7 op_sel:[0,0,1]
	v_mul_f32_e32 v6, 0x42800000, v17
	v_mov_b32_e32 v3, v193
	v_cvt_pk_fp8_f32 v3, v5, v6
	v_mul_f32_e32 v7, 0x42800000, v19
	v_mul_f32_e32 v8, 0x42800000, v21
	v_ashrrev_i32_e32 v5, 31, v4
	v_cvt_pk_fp8_f32 v3, v7, v8 op_sel:[0,0,1]
	v_lshlrev_b64 v[4:5], 10, v[4:5]
	v_lshl_add_u64 v[0:1], v[0:1], 0, v[4:5]
	global_store_dwordx2 v[0:1], v[2:3], off
	s_waitcnt lgkmcnt(0)
	s_cbranch_scc1 .Lg1p_1109
.Lg1p_done:
	s_mov_b32 s10, s22
	s_mov_b32 s17, s23
	s_mov_b64 s[38:39], s[24:25]
	v_mov_b32_e32 v0, v150
	v_mov_b32_e32 v1, v151
	v_mov_b32_e32 v2, v152
	v_mov_b32_e32 v3, v153
	v_mov_b32_e32 v4, v154
	v_mov_b32_e32 v5, v155
	v_mov_b32_e32 v6, v156
	v_mov_b32_e32 v7, v157
	v_mov_b32_e32 v8, v158
	v_mov_b32_e32 v9, v159
	v_mov_b32_e32 v10, v160
	v_mov_b32_e32 v11, v161
	v_mov_b32_e32 v12, v162
	v_mov_b32_e32 v13, v163
	v_mov_b32_e32 v14, v164
	v_mov_b32_e32 v15, v165
	v_mov_b32_e32 v16, v166
	v_mov_b32_e32 v17, v167
	v_mov_b32_e32 v18, v168
	v_mov_b32_e32 v19, v169
	v_mov_b32_e32 v20, v170
	v_mov_b32_e32 v21, v171
	v_mov_b32_e32 v22, v172
	v_mov_b32_e32 v23, v173
	v_mov_b32_e32 v24, v174
	v_mov_b32_e32 v25, v175
	v_mov_b32_e32 v26, v176
	v_mov_b32_e32 v27, v177
	v_mov_b32_e32 v28, v178
	v_mov_b32_e32 v29, v179
	v_mov_b32_e32 v30, v180
	v_mov_b32_e32 v31, v181
	v_mov_b32_e32 v32, v182
	v_mov_b32_e32 v33, v183
	v_mov_b32_e32 v34, v184
	v_mov_b32_e32 v35, v185
	v_mov_b32_e32 v36, v186
	v_mov_b32_e32 v37, v187
	v_mov_b32_e32 v38, v188
	v_mov_b32_e32 v39, v189
	v_mov_b32_e32 v40, v190
	v_mov_b32_e32 v41, v191
	v_mov_b32_e32 v192, v194
	s_waitcnt lgkmcnt(0)
	s_barrier
.Lg1p_skip:
	s_and_b64 s[4:5], s[56:57], exec
	s_movk_i32 s2, 0xb00
	s_cselect_b32 s7, s2, 0x500
	s_mov_b64 s[4:5], s[58:59]
	v_readlane_b32 s2, v252, 0
	s_waitcnt lgkmcnt(0)
	v_mbcnt_lo_u32_b32 v0, -1, 0
	v_mbcnt_hi_u32_b32 v0, -1, v0
	s_lshr_b32 s28, s7, 1
	s_mov_b32 s8, s60
	v_add_u32_e32 v4, s2, v0
	s_mov_b32 s2, s94
	s_cmp_ge_i32 s94, s28
	v_mov_b32_e32 v230, 0x79797979
	v_readfirstlane_b32 s2, v4
	v_mov_b32_e32 v231, 0x7f7f7f7f
	s_cbranch_scc1 .LBB0_186
	s_load_dwordx2 s[4:5], s[4:5], 0x128
	s_lshr_b32 s9, s7, 9
	v_readlane_b32 s12, v253, 54
	s_lshr_b32 s6, s7, 8
	s_or_b32 s10, s9, 32
	s_mul_i32 s9, s12, 0x2c0000
	v_readlane_b32 s13, v253, 55
	s_waitcnt lgkmcnt(0)
	s_add_u32 s9, s4, s9
	s_addc_u32 s13, s5, 0
	v_cvt_f32_ubyte1_e32 v0, s7
	s_add_u32 s19, s9, 0xc00000
	v_rcp_iflag_f32_e32 v1, v0
	s_mul_i32 s12, s12, 0x140000
	s_addc_u32 s9, s13, 0
	s_add_u32 s12, s4, s12
	s_addc_u32 s13, s5, 0
	v_cvt_f32_ubyte0_e32 v2, s10
	s_add_u32 s12, s12, 0x1c00000
	v_mul_f32_e32 v1, v2, v1
	s_addc_u32 s13, s13, 0
	v_trunc_f32_e32 v1, v1
	s_and_b64 s[22:23], s[56:57], exec
	v_cvt_u32_f32_e32 v3, v1
	v_fma_f32 v1, -v1, v0, v2
	v_cmp_ge_f32_e64 s[22:23], |v1|, v0
	v_lshlrev_b32_e32 v0, 4, v4
	v_add_u32_e32 v1, 0x2000, v0
	v_ashrrev_i32_e32 v2, 31, v1
	v_lshrrev_b32_e32 v2, 22, v2
	v_add_u32_e32 v2, v1, v2
	v_ashrrev_i32_e32 v2, 10, v2
	v_readfirstlane_b32 s10, v3
	v_mul_i32_i24_e32 v3, 0x400, v2
	v_sub_u32_e32 v1, v1, v3
	v_lshrrev_b32_e32 v3, 4, v1
	v_bitop3_b32 v1, v3, v1, 32 bitop3:0x6c
	v_ashrrev_i32_e32 v3, 31, v1
	v_lshrrev_b32_e32 v3, 26, v3
	v_add_u32_e32 v3, v1, v3
	v_ashrrev_i32_e32 v5, 6, v3
	v_and_b32_e32 v3, 0xc0, v3
	v_sub_u32_e32 v1, v1, v3
	v_lshlrev_b32_e32 v6, 3, v2
	v_lshlrev_b32_e32 v2, 5, v2
	v_ashrrev_i16_sdwa v1, v222, sext(v1) dst_sel:DWORD dst_unused:UNUSED_PAD src0_sel:DWORD src1_sel:BYTE_0
	v_and_b32_e32 v2, 32, v2
	v_bfe_i32 v1, v1, 0, 16
	v_and_b32_e32 v7, -16, v6
	v_add_lshl_u32 v1, v2, v1, 1
	v_bfe_i32 v2, v4, 27, 1
	s_cselect_b32 s19, s19, s12
	v_add_u32_e32 v7, v5, v7
	v_and_b32_e32 v8, 3, v5
	s_mov_b32 s12, 0x3fffe0
	v_lshrrev_b32_e32 v2, 22, v2
	v_and_or_b32 v8, v7, s12, v8
	v_lshrrev_b32_e32 v9, 2, v7
	v_lshlrev_b32_e32 v7, 1, v7
	v_add_u32_e32 v2, v0, v2
	v_and_b32_e32 v9, 4, v9
	v_and_b32_e32 v7, 24, v7
	v_and_b32_e32 v2, 0xfffffc00, v2
	v_or3_b32 v7, v8, v9, v7
	v_sub_u32_e32 v0, v0, v2
	v_lshl_add_u32 v202, v7, 10, v1
	v_lshrrev_b32_e32 v2, 4, v0
	v_ashrrev_i32_e32 v7, 31, v4
	v_bitop3_b32 v0, v2, v0, 32 bitop3:0x6c
	v_lshrrev_b32_e32 v7, 26, v7
	v_ashrrev_i32_e32 v2, 31, v0
	v_add_u32_e32 v7, v4, v7
	s_cselect_b32 s9, s9, s13
	s_add_u32 s42, s4, 0xec000000
	v_lshrrev_b32_e32 v2, 26, v2
	v_ashrrev_i32_e32 v7, 6, v7
	s_addc_u32 s43, s5, 0
	v_add_u32_e32 v2, v0, v2
	v_lshlrev_b32_e32 v8, 3, v7
	s_cmp_lg_u64 s[22:23], 0
	v_ashrrev_i32_e32 v3, 6, v2
	v_and_b32_e32 v9, -16, v8
	s_addc_u32 s10, s10, 0
	v_add_u32_e32 v9, v3, v9
	v_and_b32_e32 v10, 3, v3
	s_and_b32 s22, s10, 63
	s_ashr_i32 s10, s2, 6
	s_lshr_b32 s24, s7, 4
	v_and_or_b32 v10, v9, s12, v10
	v_readlane_b32 s12, v253, 16
	s_ashr_i32 s36, s2, 8
	s_lshl_b32 s23, s10, 10
	s_or_b32 s25, s24, 1
	v_readlane_b32 s13, v253, 17
	s_and_b64 s[30:31], s[12:13], exec
	s_mul_i32 s30, s6, s22
	v_and_b32_e32 v2, 0xc0, v2
	s_cselect_b32 s12, s25, s24
	s_abs_i32 s31, s30
	v_sub_u32_e32 v0, v0, v2
	v_cvt_f32_u32_e32 v2, s31
	v_readlane_b32 s6, v253, 18
	s_sub_i32 s37, 0, s31
	s_mul_i32 s6, s12, s6
	v_rcp_iflag_f32_e32 v2, v2
	v_readlane_b32 s12, v253, 19
	s_add_i32 s6, s6, s12
	s_abs_i32 s13, s6
	v_mul_f32_e32 v2, 0x4f7ffffe, v2
	v_cvt_u32_f32_e32 v2, v2
	s_ashr_i32 s12, s6, 31
	s_ashr_i32 s60, s30, 31
	s_xor_b32 s12, s12, s60
	v_readfirstlane_b32 s61, v2
	s_mul_i32 s37, s37, s61
	s_mul_hi_u32 s37, s61, s37
	s_add_i32 s61, s61, s37
	s_mul_hi_u32 s37, s13, s61
	s_mul_i32 s44, s37, s31
	s_sub_i32 s13, s13, s44
	s_add_i32 s44, s37, 1
	s_sub_i32 s45, s13, s31
	s_cmp_ge_u32 s13, s31
	s_cselect_b32 s37, s44, s37
	s_cselect_b32 s13, s45, s13
	s_add_i32 s44, s37, 1
	s_cmp_ge_u32 s13, s31
	s_cselect_b32 s13, s44, s37
	s_xor_b32 s13, s13, s12
	s_sub_i32 s12, s13, s12
	s_mul_i32 s13, s12, s22
	s_sub_i32 s37, 0x80, s13
	s_min_i32 s37, s37, s22
	s_sext_i32_i16 s44, s37
	v_cvt_f32_i32_e32 v2, s44
	v_lshrrev_b32_e32 v11, 2, v9
	v_lshlrev_b32_e32 v9, 1, v9
	v_lshlrev_b32_e32 v7, 5, v7
	v_ashrrev_i16_sdwa v0, v222, sext(v0) dst_sel:DWORD dst_unused:UNUSED_PAD src0_sel:DWORD src1_sel:BYTE_0
	v_and_b32_e32 v11, 4, v11
	v_and_b32_e32 v9, 24, v9
	v_and_b32_e32 v7, 32, v7
	v_bfe_i32 v0, v0, 0, 16
	s_mul_i32 s12, s12, s30
	v_or3_b32 v9, v10, v11, v9
	v_add_lshl_u32 v0, v7, v0, 1
	s_sub_i32 s12, s6, s12
	v_lshl_add_u32 v204, v9, 10, v0
	v_cvt_f32_i32_e32 v7, s12
	v_rcp_iflag_f32_e32 v9, v2
	s_xor_b32 s6, s12, s44
	s_ashr_i32 s6, s6, 30
	s_or_b32 s6, s6, 1
	v_mul_f32_e32 v9, v7, v9
	v_trunc_f32_e32 v9, v9
	v_fma_f32 v7, -v9, v2, v7
	v_cvt_i32_f32_e32 v9, v9
	v_cmp_ge_f32_e64 s[44:45], |v7|, |v2|
	s_and_b64 s[44:45], s[44:45], exec
	s_cselect_b32 s6, s6, 0
	v_readfirstlane_b32 s44, v9
	s_add_i32 s6, s44, s6
	s_mul_i32 s37, s6, s37
	s_sub_i32 s12, s12, s37
	s_sext_i32_i16 s12, s12
	s_add_i32 s75, s13, s12
	s_bfe_i64 s[44:45], s[6:7], 0x100000
	s_lshl_b32 s12, s75, 18
	s_lshl_b64 s[44:45], s[44:45], 18
	s_mov_b64 s[88:89], s[56:57]
	s_add_u32 s56, s19, s44
	s_addc_u32 s57, s9, s45
	s_add_i32 s62, s23, 0
	s_add_i32 s63, s62, 0x10000
	s_add_i32 s64, s62, 0x12000
	v_and_b32_e32 v2, 0x3ffff0, v8
	s_mov_b32 m0, s63
	s_add_u32 s44, s56, 0x20000
	v_add_u32_e32 v2, v3, v2
	global_load_lds_dwordx4 v204, s[56:57]
	s_mov_b32 m0, s64
	s_addc_u32 s45, s57, 0
	s_add_i32 s65, s62, 0x14000
	v_lshl_add_u32 v232, v2, 10, v0
	v_and_b32_e32 v0, 0x3ffff0, v6
	global_load_lds_dwordx4 v202, s[56:57]
	s_mov_b32 m0, s65
	s_add_i32 s66, s62, 0x16000
	v_add_u32_e32 v0, v5, v0
	global_load_lds_dwordx4 v204, s[44:45]
	s_mov_b32 m0, s66
	v_add_u32_e32 v192, s12, v232
	v_lshl_add_u32 v234, v0, 10, v1
	global_load_lds_dwordx4 v202, s[44:45]
	s_mov_b32 m0, s62
	s_add_i32 s67, s62, 0x2000
	v_add_u32_e32 v233, 0x20000, v232
	v_add_u32_e32 v210, s12, v234
	global_load_lds_dwordx4 v192, s[42:43]
	s_mov_b32 m0, s67
	s_add_i32 s68, s62, 0x4000
	v_add_u32_e32 v206, s12, v233
	v_add_u32_e32 v235, 0x20000, v234
	global_load_lds_dwordx4 v210, s[42:43]
	s_mov_b32 m0, s68
	s_add_i32 s69, s62, 0x6000
	v_add_u32_e32 v208, s12, v235
	global_load_lds_dwordx4 v206, s[42:43]
	s_mov_b32 m0, s69
	v_mov_b32_e32 v205, v193
	global_load_lds_dwordx4 v208, s[42:43]
	v_mov_b32_e32 v203, v193
	s_cmp_eq_u32 s36, 1
	v_lshl_add_u64 v[0:1], s[56:57], 0, v[204:205]
	s_cselect_b64 s[44:45], -1, 0
	s_cmp_lg_u32 s36, 1
	v_lshl_add_u64 v[2:3], s[56:57], 0, v[202:203]
	s_cbranch_scc1 .LBB0_170
	s_barrier

; #define LAS __attribute__((address_space(3)))
; DI void phase_expert_weights(const Frame& F, int l, int which) {
;     LAS float* scr = (LAS float*)(F.lds + F.wave * 16384);
;     unsigned char* ws = F.ws;
;     if (which == 0) {
;         constexpr int IPM = (D / 64) * (2048 / 32);
;         for (int it = F.gw; it < NE * IPM; it += F.NGW) { const int mtx = l * NE + it / IPM, r = it % IPM;
;             transpose_item(F.ap->in[32] + (size_t)mtx * D * 2048, D, 2048, (bf16_t*)(ws + WS_W1 + (size_t)mtx * 2048 * D), 3, scr, r, F.lane); }
.LBB0_186:
	s_bitcmp1_b32 s94, 0
	s_cbranch_scc1 .Lg1c_skip
	s_mov_b32 s22, s10
	s_mov_b32 s23, s17
	s_mov_b64 s[24:25], s[38:39]
	v_readlane_b32 s30, v253, 58
	s_nop 0
	s_lshl_b32 s30, s30, 1
	v_mov_b32_e32 v150, v0
	v_mov_b32_e32 v151, v1
	v_mov_b32_e32 v152, v2
	v_mov_b32_e32 v153, v3
	v_mov_b32_e32 v154, v4
	v_mov_b32_e32 v155, v5
	v_mov_b32_e32 v156, v6
	v_mov_b32_e32 v157, v7
	v_mov_b32_e32 v158, v8
	v_mov_b32_e32 v159, v9
	v_mov_b32_e32 v160, v10
	v_mov_b32_e32 v161, v11
	v_mov_b32_e32 v162, v12
	v_mov_b32_e32 v163, v13
	v_mov_b32_e32 v164, v14
	v_mov_b32_e32 v165, v15
	v_mov_b32_e32 v166, v16
	v_mov_b32_e32 v167, v17
	v_mov_b32_e32 v168, v18
	v_mov_b32_e32 v169, v19
	v_mov_b32_e32 v170, v20
	v_mov_b32_e32 v171, v21
	v_mov_b32_e32 v172, v22
	v_mov_b32_e32 v173, v23
	v_mov_b32_e32 v174, v24
	v_mov_b32_e32 v175, v25
	v_mov_b32_e32 v176, v26
	v_mov_b32_e32 v177, v27
	v_mov_b32_e32 v178, v28
	v_mov_b32_e32 v179, v29
	v_mov_b32_e32 v180, v30
	v_mov_b32_e32 v181, v31
	v_mov_b32_e32 v182, v32
	v_mov_b32_e32 v183, v33
	v_mov_b32_e32 v184, v34
	v_mov_b32_e32 v185, v35
	v_mov_b32_e32 v186, v36
	v_mov_b32_e32 v187, v37
	v_mov_b32_e32 v188, v38
	v_mov_b32_e32 v189, v39
	v_mov_b32_e32 v190, v40
	v_mov_b32_e32 v191, v41
	v_mov_b32_e32 v194, v192
	s_mov_b64 s[4:5], s[58:59]
	v_readlane_b32 s2, v252, 0
	s_waitcnt lgkmcnt(0)
	v_mbcnt_lo_u32_b32 v0, -1, 0
	v_mbcnt_hi_u32_b32 v0, -1, v0
	s_mov_b32 s6, s94
	v_add_u32_e32 v1, s2, v0
	s_mov_b32 s2, s60
	s_and_b32 s7, s2, 7
	s_cmp_lg_u32 s7, 0
	v_readfirstlane_b32 s7, v1
	s_cbranch_scc1 .Lg1c_1107
	s_ashr_i32 s9, s6, 31
	s_lshr_b32 s9, s9, 29
	s_add_i32 s9, s6, s9
	s_ashr_i32 s10, s9, 3
	s_and_b32 s9, s9, -8
	s_ashr_i32 s8, s2, 3
	s_sub_i32 s6, s6, s9
	s_mul_i32 s6, s8, s6
	s_add_i32 s6, s6, s10

; #define LAS __attribute__((address_space(3)))
; DI void phase_expert_weights(const Frame& F, int l, int which) {
;     LAS float* scr = (LAS float*)(F.lds + F.wave * 16384);
;     unsigned char* ws = F.ws;
;     if (which == 0) {
;         constexpr int IPM = (D / 64) * (2048 / 32);
;         for (int it = F.gw; it < NE * IPM; it += F.NGW) { const int mtx = l * NE + it / IPM, r = it % IPM;
;             transpose_item(F.ap->in[32] + (size_t)mtx * D * 2048, D, 2048, (bf16_t*)(ws + WS_W1 + (size_t)mtx * 2048 * D), 3, scr, r, F.lane); }
.Lg1c_done:
	s_mov_b32 s10, s22
	s_mov_b32 s17, s23
	s_mov_b64 s[38:39], s[24:25]
	v_mov_b32_e32 v0, v150
	v_mov_b32_e32 v1, v151
	v_mov_b32_e32 v2, v152
	v_mov_b32_e32 v3, v153
	v_mov_b32_e32 v4, v154
	v_mov_b32_e32 v5, v155
	v_mov_b32_e32 v6, v156
	v_mov_b32_e32 v7, v157
	v_mov_b32_e32 v8, v158
	v_mov_b32_e32 v9, v159
	v_mov_b32_e32 v10, v160
	v_mov_b32_e32 v11, v161
	v_mov_b32_e32 v12, v162
	v_mov_b32_e32 v13, v163
	v_mov_b32_e32 v14, v164
	v_mov_b32_e32 v15, v165
	v_mov_b32_e32 v16, v166
	v_mov_b32_e32 v17, v167
	v_mov_b32_e32 v18, v168
	v_mov_b32_e32 v19, v169
	v_mov_b32_e32 v20, v170
	v_mov_b32_e32 v21, v171
	v_mov_b32_e32 v22, v172
	v_mov_b32_e32 v23, v173
	v_mov_b32_e32 v24, v174
	v_mov_b32_e32 v25, v175
	v_mov_b32_e32 v26, v176
	v_mov_b32_e32 v27, v177
	v_mov_b32_e32 v28, v178
	v_mov_b32_e32 v29, v179
	v_mov_b32_e32 v30, v180
	v_mov_b32_e32 v31, v181
	v_mov_b32_e32 v32, v182
	v_mov_b32_e32 v33, v183
	v_mov_b32_e32 v34, v184
	v_mov_b32_e32 v35, v185
	v_mov_b32_e32 v36, v186
	v_mov_b32_e32 v37, v187
	v_mov_b32_e32 v38, v188
	v_mov_b32_e32 v39, v189
	v_mov_b32_e32 v40, v190
	v_mov_b32_e32 v41, v191
	v_mov_b32_e32 v192, v194

; #define REP(n) for (int rep_ = 0; rep_ < 1 + ((REPMASK >> (n)) & 1); ++rep_)
; #define IN(k) (lo <= (k) && (k) < hi && ((F = make_frame((LAS unsigned char*)lds_raw, wv)), true))
; #define SEAM(k) do { if ((k) + 1 < hi) xcd_barrier(bar, tid_now(wv) == 0); } while (0)
; __global__ void __launch_bounds__(NTHR, 2) fwd_kernel(Args args) {
;     ...
;         REP(11) if (PM(11)) if (IN(pb + 8)) { phase_tail(F, l); SEAM(pb + 8); }
;         if (IN(pb + 9)) { phase_expert_weights(F, l, 0); SEAM(pb + 9); }
.LBB0_1104:
	v_readlane_b32 s50, v253, 50
	s_andn2_b64 vcc, exec, s[4:5]
	v_readlane_b32 s51, v253, 51
	s_cbranch_vccnz .LBB0_1160
	s_branch .LBB0_1110
	s_mov_b64 s[4:5], s[58:59]
	v_readlane_b32 s2, v252, 0
	s_waitcnt lgkmcnt(0)
	v_mbcnt_lo_u32_b32 v0, -1, 0
	v_mbcnt_hi_u32_b32 v0, -1, v0
	s_mov_b32 s6, s94
	v_add_u32_e32 v1, s2, v0
	s_mov_b32 s2, s60
	s_and_b32 s7, s2, 7
	s_cmp_lg_u32 s7, 0
	v_readfirstlane_b32 s7, v1
	s_cbranch_scc1 .LBB0_1107
	s_ashr_i32 s9, s6, 31
	s_lshr_b32 s9, s9, 29
	s_add_i32 s9, s6, s9
	s_ashr_i32 s10, s9, 3
	s_and_b32 s9, s9, -8
	s_ashr_i32 s8, s2, 3
	s_sub_i32 s6, s6, s9
	s_mul_i32 s6, s8, s6
	s_add_i32 s6, s6, s10
